# v56 + cache policy: gate/up epilogue stores of hid marked nt (sc1 nt) so they do not displace the A/B tiles in L2
# baseline (speedup 1.0000x reference)
; __device__ __forceinline__ float sigm(float x) { return __builtin_amdgcn_rcpf(1.0f + __builtin_amdgcn_exp2f(-1.4426950408889634f * x)); }
; __device__ __forceinline__ u32x4 pack8(const f32x4 a, const f32x4 b) { u32x4 w; w.x = cvt_pk_bf16(a[0], a[1]); w.y = cvt_pk_bf16(a[2], a[3]); w.z = cvt_pk_bf16(b[0], b[1]); w.w = cvt_pk_bf16(b[2], b[3]); return w; }
;     __device__ __forceinline__ void operator()(const f32x4 (&acc)[2][2][4][2], const Unit& u, int wr, int wc, int fr, int fq) const {
;         const int row0 = u.pm * BM + wr * 64 + fr, col0 = u.pn * HALF + wc * 32 + 8 * fq;
; #pragma unroll
;         for (int ai = 0; ai < 2; ++ai)
; #pragma unroll
;             for (int m = 0; m < 4; ++m) {
;                 bf16_t* rowp = O + (size_t)(row0 + ai * HALF + m * 16) * ldc + col0;
;                 f32x4 h[2];
; #pragma unroll
;                 for (int n = 0; n < 2; ++n) { const f32x4 gt = acc[ai][0][m][n], up = acc[ai][1][m][n];
; #pragma unroll
;                     for (int e = 0; e < 4; ++e) h[n][e] = gt[e] * sigm(gt[e]) * up[e]; }
;                 *(u32x4*)rowp = pack8(h[0], h[1]);
;             }
.LBB0_156:
	v_pk_mul_f32 v[160:161], v[128:129], s[82:83] op_sel:[0,1] op_sel_hi:[1,1]
	v_pk_mul_f32 v[162:163], v[130:131], s[82:83] op_sel:[0,1] op_sel_hi:[1,1]
	v_pk_mul_f32 v[164:165], v[120:121], s[82:83] op_sel:[0,1] op_sel_hi:[1,1]
	v_pk_mul_f32 v[166:167], v[122:123], s[82:83] op_sel:[0,1] op_sel_hi:[1,1]
	v_exp_f32_e32 v160, v160
	v_exp_f32_e32 v161, v161
	v_exp_f32_e32 v162, v162
	v_exp_f32_e32 v163, v163
	v_exp_f32_e32 v164, v164
	v_exp_f32_e32 v165, v165
	v_exp_f32_e32 v166, v166
	v_exp_f32_e32 v167, v167
	v_pk_add_f32 v[160:161], v[160:161], 1.0 op_sel_hi:[1,0]
	v_pk_add_f32 v[162:163], v[162:163], 1.0 op_sel_hi:[1,0]
	v_pk_add_f32 v[164:165], v[164:165], 1.0 op_sel_hi:[1,0]
	v_pk_add_f32 v[166:167], v[166:167], 1.0 op_sel_hi:[1,0]
	v_rcp_f32_e32 v160, v160
	v_rcp_f32_e32 v161, v161
	v_rcp_f32_e32 v162, v162
	v_rcp_f32_e32 v163, v163
	v_rcp_f32_e32 v164, v164
	v_rcp_f32_e32 v165, v165
	v_rcp_f32_e32 v166, v166
	v_rcp_f32_e32 v167, v167
	v_pk_mul_f32 v[160:161], v[128:129], v[160:161]
	v_pk_mul_f32 v[162:163], v[130:131], v[162:163]
	v_pk_mul_f32 v[164:165], v[120:121], v[164:165]
	v_pk_mul_f32 v[166:167], v[122:123], v[166:167]
	v_pk_mul_f32 v[124:125], v[160:161], v[124:125]
	v_pk_mul_f32 v[126:127], v[162:163], v[126:127]
	v_pk_mul_f32 v[120:121], v[164:165], v[116:117]
	v_pk_mul_f32 v[128:129], v[166:167], v[118:119]
	v_lshl_or_b32 v152, s21, 7, v148
	v_lshl_add_u32 v150, s20, 8, v2
	v_ashrrev_i32_e32 v153, 31, v152
	v_mov_b64_e32 v[144:145], s[8:9]
	v_mad_i64_i32 v[154:155], s[20:21], v150, s82, v[144:145]
	s_andn2_b64 vcc, exec, s[2:3]
	v_lshlrev_b64 v[116:117], 1, v[152:153]
	v_lshl_add_u64 v[122:123], v[154:155], 0, v[116:117]
	v_cvt_pk_bf16_f32 v118, v124, v125
	v_cvt_pk_bf16_f32 v119, v126, v127
	v_cvt_pk_bf16_f32 v120, v120, v121
	v_cvt_pk_bf16_f32 v121, v128, v129
	flat_store_dwordx4 v[122:123], v[118:121] sc1 nt
	s_nop 1
	v_pk_mul_f32 v[160:161], v[112:113], s[82:83] op_sel:[0,1] op_sel_hi:[1,1]
	v_pk_mul_f32 v[162:163], v[114:115], s[82:83] op_sel:[0,1] op_sel_hi:[1,1]
	v_pk_mul_f32 v[164:165], v[104:105], s[82:83] op_sel:[0,1] op_sel_hi:[1,1]
	v_pk_mul_f32 v[166:167], v[106:107], s[82:83] op_sel:[0,1] op_sel_hi:[1,1]
	v_exp_f32_e32 v160, v160
	v_exp_f32_e32 v161, v161
	v_exp_f32_e32 v162, v162
	v_exp_f32_e32 v163, v163
	v_exp_f32_e32 v164, v164
	v_exp_f32_e32 v165, v165
	v_exp_f32_e32 v166, v166
	v_exp_f32_e32 v167, v167
	v_pk_add_f32 v[160:161], v[160:161], 1.0 op_sel_hi:[1,0]
	v_pk_add_f32 v[162:163], v[162:163], 1.0 op_sel_hi:[1,0]
	v_pk_add_f32 v[164:165], v[164:165], 1.0 op_sel_hi:[1,0]
	v_pk_add_f32 v[166:167], v[166:167], 1.0 op_sel_hi:[1,0]
	v_rcp_f32_e32 v160, v160
	v_rcp_f32_e32 v161, v161
	v_rcp_f32_e32 v162, v162
	v_rcp_f32_e32 v163, v163
	v_rcp_f32_e32 v164, v164
	v_rcp_f32_e32 v165, v165
	v_rcp_f32_e32 v166, v166
	v_rcp_f32_e32 v167, v167
	v_pk_mul_f32 v[160:161], v[112:113], v[160:161]
	v_pk_mul_f32 v[162:163], v[114:115], v[162:163]
	v_pk_mul_f32 v[164:165], v[104:105], v[164:165]
	v_pk_mul_f32 v[166:167], v[106:107], v[166:167]
	v_pk_mul_f32 v[108:109], v[160:161], v[108:109]
	v_pk_mul_f32 v[110:111], v[162:163], v[110:111]
	v_pk_mul_f32 v[112:113], v[164:165], v[100:101]
	v_mul_f32_e32 v106, v166, v102
	v_mul_f32_e32 v103, v167, v103
	v_or_b32_e32 v118, 16, v150
	v_mad_i64_i32 v[118:119], s[20:21], v118, s82, v[144:145]
	v_lshl_add_u64 v[104:105], v[118:119], 0, v[116:117]
	v_cvt_pk_bf16_f32 v100, v108, v109
	v_cvt_pk_bf16_f32 v101, v110, v111
	v_cvt_pk_bf16_f32 v102, v112, v113
	v_cvt_pk_bf16_f32 v103, v106, v103
	flat_store_dwordx4 v[104:105], v[100:103] sc1 nt
	s_nop 1
	v_pk_mul_f32 v[160:161], v[96:97], s[82:83] op_sel:[0,1] op_sel_hi:[1,1]
	v_pk_mul_f32 v[162:163], v[98:99], s[82:83] op_sel:[0,1] op_sel_hi:[1,1]
	v_pk_mul_f32 v[164:165], v[88:89], s[82:83] op_sel:[0,1] op_sel_hi:[1,1]
	v_pk_mul_f32 v[166:167], v[90:91], s[82:83] op_sel:[0,1] op_sel_hi:[1,1]
	v_exp_f32_e32 v160, v160
	v_exp_f32_e32 v161, v161
	v_exp_f32_e32 v162, v162
	v_exp_f32_e32 v163, v163
	v_exp_f32_e32 v164, v164
	v_exp_f32_e32 v165, v165
	v_exp_f32_e32 v166, v166
	v_exp_f32_e32 v167, v167
	v_pk_add_f32 v[160:161], v[160:161], 1.0 op_sel_hi:[1,0]
	v_pk_add_f32 v[162:163], v[162:163], 1.0 op_sel_hi:[1,0]
	v_pk_add_f32 v[164:165], v[164:165], 1.0 op_sel_hi:[1,0]
	v_pk_add_f32 v[166:167], v[166:167], 1.0 op_sel_hi:[1,0]
	v_rcp_f32_e32 v160, v160
	v_rcp_f32_e32 v161, v161
	v_rcp_f32_e32 v162, v162
	v_rcp_f32_e32 v163, v163
	v_rcp_f32_e32 v164, v164
	v_rcp_f32_e32 v165, v165
	v_rcp_f32_e32 v166, v166
	v_rcp_f32_e32 v167, v167
	v_pk_mul_f32 v[160:161], v[96:97], v[160:161]
	v_pk_mul_f32 v[162:163], v[98:99], v[162:163]
	v_pk_mul_f32 v[164:165], v[88:89], v[164:165]
	v_pk_mul_f32 v[166:167], v[90:91], v[166:167]
	v_pk_mul_f32 v[92:93], v[160:161], v[92:93]
	v_pk_mul_f32 v[94:95], v[162:163], v[94:95]
	v_pk_mul_f32 v[96:97], v[164:165], v[84:85]
	v_mul_f32_e32 v90, v166, v86
	v_mul_f32_e32 v87, v167, v87
	v_or_b32_e32 v100, 32, v150
	v_mad_i64_i32 v[100:101], s[20:21], v100, s82, v[144:145]
	v_lshl_add_u64 v[88:89], v[100:101], 0, v[116:117]
	v_cvt_pk_bf16_f32 v84, v92, v93
	v_cvt_pk_bf16_f32 v85, v94, v95
	v_cvt_pk_bf16_f32 v86, v96, v97
	v_cvt_pk_bf16_f32 v87, v90, v87
	flat_store_dwordx4 v[88:89], v[84:87] sc1 nt
	s_nop 1
	v_pk_mul_f32 v[160:161], v[80:81], s[82:83] op_sel:[0,1] op_sel_hi:[1,1]
	v_pk_mul_f32 v[162:163], v[82:83], s[82:83] op_sel:[0,1] op_sel_hi:[1,1]
	v_pk_mul_f32 v[164:165], v[72:73], s[82:83] op_sel:[0,1] op_sel_hi:[1,1]
	v_pk_mul_f32 v[166:167], v[74:75], s[82:83] op_sel:[0,1] op_sel_hi:[1,1]
	v_exp_f32_e32 v160, v160
	v_exp_f32_e32 v161, v161
	v_exp_f32_e32 v162, v162
	v_exp_f32_e32 v163, v163
; __device__ __forceinline__ float sigm(float x) { return __builtin_amdgcn_rcpf(1.0f + __builtin_amdgcn_exp2f(-1.4426950408889634f * x)); }
; __device__ __forceinline__ u32x4 pack8(const f32x4 a, const f32x4 b) { u32x4 w; w.x = cvt_pk_bf16(a[0], a[1]); w.y = cvt_pk_bf16(a[2], a[3]); w.z = cvt_pk_bf16(b[0], b[1]); w.w = cvt_pk_bf16(b[2], b[3]); return w; }
;     __device__ __forceinline__ void operator()(const f32x4 (&acc)[2][2][4][2], const Unit& u, int wr, int wc, int fr, int fq) const {
;         const int row0 = u.pm * BM + wr * 64 + fr, col0 = u.pn * HALF + wc * 32 + 8 * fq;
; #pragma unroll
;         for (int ai = 0; ai < 2; ++ai)
; #pragma unroll
;             for (int m = 0; m < 4; ++m) {
;                 bf16_t* rowp = O + (size_t)(row0 + ai * HALF + m * 16) * ldc + col0;
;                 f32x4 h[2];
; #pragma unroll
;                 for (int n = 0; n < 2; ++n) { const f32x4 gt = acc[ai][0][m][n], up = acc[ai][1][m][n];
; #pragma unroll
;                     for (int e = 0; e < 4; ++e) h[n][e] = gt[e] * sigm(gt[e]) * up[e]; }
;                 *(u32x4*)rowp = pack8(h[0], h[1]);
;             }
	v_exp_f32_e32 v164, v164
	v_exp_f32_e32 v165, v165
	v_exp_f32_e32 v166, v166
	v_exp_f32_e32 v167, v167
	v_pk_add_f32 v[160:161], v[160:161], 1.0 op_sel_hi:[1,0]
	v_pk_add_f32 v[162:163], v[162:163], 1.0 op_sel_hi:[1,0]
	v_pk_add_f32 v[164:165], v[164:165], 1.0 op_sel_hi:[1,0]
	v_pk_add_f32 v[166:167], v[166:167], 1.0 op_sel_hi:[1,0]
	v_rcp_f32_e32 v160, v160
	v_rcp_f32_e32 v161, v161
	v_rcp_f32_e32 v162, v162
	v_rcp_f32_e32 v163, v163
	v_rcp_f32_e32 v164, v164
	v_rcp_f32_e32 v165, v165
	v_rcp_f32_e32 v166, v166
	v_rcp_f32_e32 v167, v167
	v_pk_mul_f32 v[160:161], v[80:81], v[160:161]
	v_pk_mul_f32 v[162:163], v[82:83], v[162:163]
	v_pk_mul_f32 v[164:165], v[72:73], v[164:165]
	v_pk_mul_f32 v[166:167], v[74:75], v[166:167]
	v_pk_mul_f32 v[76:77], v[160:161], v[76:77]
	v_pk_mul_f32 v[78:79], v[162:163], v[78:79]
	v_pk_mul_f32 v[80:81], v[164:165], v[68:69]
	v_mul_f32_e32 v74, v166, v70
	v_mul_f32_e32 v71, v167, v71
	v_or_b32_e32 v84, 48, v150
	v_mad_i64_i32 v[84:85], s[20:21], v84, s82, v[144:145]
	v_lshl_add_u64 v[72:73], v[84:85], 0, v[116:117]
	v_cvt_pk_bf16_f32 v68, v76, v77
	v_cvt_pk_bf16_f32 v69, v78, v79
	v_cvt_pk_bf16_f32 v70, v80, v81
	v_cvt_pk_bf16_f32 v71, v74, v71
	flat_store_dwordx4 v[72:73], v[68:71] sc1 nt
	s_nop 1
	v_pk_mul_f32 v[160:161], v[64:65], s[82:83] op_sel:[0,1] op_sel_hi:[1,1]
	v_pk_mul_f32 v[162:163], v[66:67], s[82:83] op_sel:[0,1] op_sel_hi:[1,1]
	v_pk_mul_f32 v[164:165], v[56:57], s[82:83] op_sel:[0,1] op_sel_hi:[1,1]
	v_pk_mul_f32 v[166:167], v[58:59], s[82:83] op_sel:[0,1] op_sel_hi:[1,1]
	v_exp_f32_e32 v160, v160
	v_exp_f32_e32 v161, v161
	v_exp_f32_e32 v162, v162
	v_exp_f32_e32 v163, v163
	v_exp_f32_e32 v164, v164
	v_exp_f32_e32 v165, v165
	v_exp_f32_e32 v166, v166
	v_exp_f32_e32 v167, v167
	v_pk_add_f32 v[160:161], v[160:161], 1.0 op_sel_hi:[1,0]
	v_pk_add_f32 v[162:163], v[162:163], 1.0 op_sel_hi:[1,0]
	v_pk_add_f32 v[164:165], v[164:165], 1.0 op_sel_hi:[1,0]
	v_pk_add_f32 v[166:167], v[166:167], 1.0 op_sel_hi:[1,0]
	v_rcp_f32_e32 v160, v160
	v_rcp_f32_e32 v161, v161
	v_rcp_f32_e32 v162, v162
	v_rcp_f32_e32 v163, v163
	v_rcp_f32_e32 v164, v164
	v_rcp_f32_e32 v165, v165
	v_rcp_f32_e32 v166, v166
	v_rcp_f32_e32 v167, v167
	v_pk_mul_f32 v[160:161], v[64:65], v[160:161]
	v_pk_mul_f32 v[162:163], v[66:67], v[162:163]
	v_pk_mul_f32 v[164:165], v[56:57], v[164:165]
	v_pk_mul_f32 v[166:167], v[58:59], v[166:167]
	v_pk_mul_f32 v[60:61], v[160:161], v[60:61]
	v_pk_mul_f32 v[62:63], v[162:163], v[62:63]
	v_pk_mul_f32 v[64:65], v[164:165], v[52:53]
	v_mul_f32_e32 v58, v166, v54
	v_mul_f32_e32 v55, v167, v55
	v_add_u32_e32 v68, 0x80, v150
	v_mad_i64_i32 v[68:69], s[20:21], v68, s82, v[144:145]
	v_lshl_add_u64 v[56:57], v[68:69], 0, v[116:117]
	v_cvt_pk_bf16_f32 v52, v60, v61
	v_cvt_pk_bf16_f32 v53, v62, v63
	v_cvt_pk_bf16_f32 v54, v64, v65
	v_cvt_pk_bf16_f32 v55, v58, v55
	flat_store_dwordx4 v[56:57], v[52:55] sc1 nt
	s_nop 1
	v_pk_mul_f32 v[160:161], v[48:49], s[82:83] op_sel:[0,1] op_sel_hi:[1,1]
	v_pk_mul_f32 v[162:163], v[50:51], s[82:83] op_sel:[0,1] op_sel_hi:[1,1]
	v_pk_mul_f32 v[164:165], v[40:41], s[82:83] op_sel:[0,1] op_sel_hi:[1,1]
	v_pk_mul_f32 v[166:167], v[42:43], s[82:83] op_sel:[0,1] op_sel_hi:[1,1]
	v_exp_f32_e32 v160, v160
	v_exp_f32_e32 v161, v161
	v_exp_f32_e32 v162, v162
	v_exp_f32_e32 v163, v163
	v_exp_f32_e32 v164, v164
	v_exp_f32_e32 v165, v165
	v_exp_f32_e32 v166, v166
	v_exp_f32_e32 v167, v167
	v_pk_add_f32 v[160:161], v[160:161], 1.0 op_sel_hi:[1,0]
	v_pk_add_f32 v[162:163], v[162:163], 1.0 op_sel_hi:[1,0]
	v_pk_add_f32 v[164:165], v[164:165], 1.0 op_sel_hi:[1,0]
	v_pk_add_f32 v[166:167], v[166:167], 1.0 op_sel_hi:[1,0]
	v_rcp_f32_e32 v160, v160
	v_rcp_f32_e32 v161, v161
	v_rcp_f32_e32 v162, v162
	v_rcp_f32_e32 v163, v163
	v_rcp_f32_e32 v164, v164
	v_rcp_f32_e32 v165, v165
	v_rcp_f32_e32 v166, v166
	v_rcp_f32_e32 v167, v167
	v_pk_mul_f32 v[160:161], v[48:49], v[160:161]
	v_pk_mul_f32 v[162:163], v[50:51], v[162:163]
	v_pk_mul_f32 v[164:165], v[40:41], v[164:165]
; __device__ __forceinline__ float sigm(float x) { return __builtin_amdgcn_rcpf(1.0f + __builtin_amdgcn_exp2f(-1.4426950408889634f * x)); }
; __device__ __forceinline__ u32x4 pack8(const f32x4 a, const f32x4 b) { u32x4 w; w.x = cvt_pk_bf16(a[0], a[1]); w.y = cvt_pk_bf16(a[2], a[3]); w.z = cvt_pk_bf16(b[0], b[1]); w.w = cvt_pk_bf16(b[2], b[3]); return w; }
;     __device__ __forceinline__ void operator()(const f32x4 (&acc)[2][2][4][2], const Unit& u, int wr, int wc, int fr, int fq) const {
;         const int row0 = u.pm * BM + wr * 64 + fr, col0 = u.pn * HALF + wc * 32 + 8 * fq;
; #pragma unroll
;         for (int ai = 0; ai < 2; ++ai)
; #pragma unroll
;             for (int m = 0; m < 4; ++m) {
;                 bf16_t* rowp = O + (size_t)(row0 + ai * HALF + m * 16) * ldc + col0;
;                 f32x4 h[2];
; #pragma unroll
;                 for (int n = 0; n < 2; ++n) { const f32x4 gt = acc[ai][0][m][n], up = acc[ai][1][m][n];
; #pragma unroll
;                     for (int e = 0; e < 4; ++e) h[n][e] = gt[e] * sigm(gt[e]) * up[e]; }
;                 *(u32x4*)rowp = pack8(h[0], h[1]);
;             }
	v_pk_mul_f32 v[166:167], v[42:43], v[166:167]
	v_pk_mul_f32 v[44:45], v[160:161], v[44:45]
	v_pk_mul_f32 v[46:47], v[162:163], v[46:47]
	v_pk_mul_f32 v[48:49], v[164:165], v[36:37]
	v_mul_f32_e32 v42, v166, v38
	v_mul_f32_e32 v39, v167, v39
	v_add_u32_e32 v52, 0x90, v150
	v_mad_i64_i32 v[52:53], s[20:21], v52, s82, v[144:145]
	v_lshl_add_u64 v[40:41], v[52:53], 0, v[116:117]
	v_cvt_pk_bf16_f32 v36, v44, v45
	v_cvt_pk_bf16_f32 v37, v46, v47
	v_cvt_pk_bf16_f32 v38, v48, v49
	v_cvt_pk_bf16_f32 v39, v42, v39
	flat_store_dwordx4 v[40:41], v[36:39] sc1 nt
	s_nop 1
	v_pk_mul_f32 v[160:161], v[32:33], s[82:83] op_sel:[0,1] op_sel_hi:[1,1]
	v_pk_mul_f32 v[162:163], v[34:35], s[82:83] op_sel:[0,1] op_sel_hi:[1,1]
	v_pk_mul_f32 v[164:165], v[24:25], s[82:83] op_sel:[0,1] op_sel_hi:[1,1]
	v_pk_mul_f32 v[166:167], v[26:27], s[82:83] op_sel:[0,1] op_sel_hi:[1,1]
	v_exp_f32_e32 v160, v160
	v_exp_f32_e32 v161, v161
	v_exp_f32_e32 v162, v162
	v_exp_f32_e32 v163, v163
	v_exp_f32_e32 v164, v164
	v_exp_f32_e32 v165, v165
	v_exp_f32_e32 v166, v166
	v_exp_f32_e32 v167, v167
	v_pk_add_f32 v[160:161], v[160:161], 1.0 op_sel_hi:[1,0]
	v_pk_add_f32 v[162:163], v[162:163], 1.0 op_sel_hi:[1,0]
	v_pk_add_f32 v[164:165], v[164:165], 1.0 op_sel_hi:[1,0]
	v_pk_add_f32 v[166:167], v[166:167], 1.0 op_sel_hi:[1,0]
	v_rcp_f32_e32 v160, v160
	v_rcp_f32_e32 v161, v161
	v_rcp_f32_e32 v162, v162
	v_rcp_f32_e32 v163, v163
	v_rcp_f32_e32 v164, v164
	v_rcp_f32_e32 v165, v165
	v_rcp_f32_e32 v166, v166
	v_rcp_f32_e32 v167, v167
	v_pk_mul_f32 v[160:161], v[32:33], v[160:161]
	v_pk_mul_f32 v[162:163], v[34:35], v[162:163]
	v_pk_mul_f32 v[164:165], v[24:25], v[164:165]
	v_pk_mul_f32 v[166:167], v[26:27], v[166:167]
	v_pk_mul_f32 v[28:29], v[160:161], v[28:29]
	v_pk_mul_f32 v[30:31], v[162:163], v[30:31]
	v_pk_mul_f32 v[32:33], v[164:165], v[20:21]
	v_mul_f32_e32 v26, v166, v22
	v_mul_f32_e32 v23, v167, v23
	v_add_u32_e32 v36, 0xa0, v150
	v_mad_i64_i32 v[36:37], s[20:21], v36, s82, v[144:145]
	v_lshl_add_u64 v[24:25], v[36:37], 0, v[116:117]
	v_cvt_pk_bf16_f32 v20, v28, v29
	v_cvt_pk_bf16_f32 v21, v30, v31
	v_cvt_pk_bf16_f32 v22, v32, v33
	v_cvt_pk_bf16_f32 v23, v26, v23
	flat_store_dwordx4 v[24:25], v[20:23] sc1 nt
	s_nop 1
	v_pk_mul_f32 v[160:161], v[16:17], s[82:83] op_sel:[0,1] op_sel_hi:[1,1]
	v_pk_mul_f32 v[162:163], v[18:19], s[82:83] op_sel:[0,1] op_sel_hi:[1,1]
	v_pk_mul_f32 v[164:165], v[8:9], s[82:83] op_sel:[0,1] op_sel_hi:[1,1]
	v_pk_mul_f32 v[166:167], v[10:11], s[82:83] op_sel:[0,1] op_sel_hi:[1,1]
	v_exp_f32_e32 v160, v160
	v_exp_f32_e32 v161, v161
	v_exp_f32_e32 v162, v162
	v_exp_f32_e32 v163, v163
	v_exp_f32_e32 v164, v164
	v_exp_f32_e32 v165, v165
	v_exp_f32_e32 v166, v166
	v_exp_f32_e32 v167, v167
	v_pk_add_f32 v[160:161], v[160:161], 1.0 op_sel_hi:[1,0]
	v_pk_add_f32 v[162:163], v[162:163], 1.0 op_sel_hi:[1,0]
	v_pk_add_f32 v[164:165], v[164:165], 1.0 op_sel_hi:[1,0]
	v_pk_add_f32 v[166:167], v[166:167], 1.0 op_sel_hi:[1,0]
	v_rcp_f32_e32 v160, v160
	v_rcp_f32_e32 v161, v161
	v_rcp_f32_e32 v162, v162
	v_rcp_f32_e32 v163, v163
	v_rcp_f32_e32 v164, v164
	v_rcp_f32_e32 v165, v165
	v_rcp_f32_e32 v166, v166
	v_rcp_f32_e32 v167, v167
	v_pk_mul_f32 v[160:161], v[16:17], v[160:161]
	v_pk_mul_f32 v[162:163], v[18:19], v[162:163]
	v_pk_mul_f32 v[164:165], v[8:9], v[164:165]
	v_pk_mul_f32 v[166:167], v[10:11], v[166:167]
	v_pk_mul_f32 v[12:13], v[160:161], v[12:13]
	v_pk_mul_f32 v[14:15], v[162:163], v[14:15]
	v_pk_mul_f32 v[16:17], v[164:165], v[4:5]
	v_mul_f32_e32 v10, v166, v6
	v_mul_f32_e32 v7, v167, v7
	v_add_u32_e32 v20, 0xb0, v150
	v_mad_i64_i32 v[20:21], s[20:21], v20, s82, v[144:145]
	s_mov_b64 s[20:21], -1
	v_lshl_add_u64 v[8:9], v[20:21], 0, v[116:117]
	v_cvt_pk_bf16_f32 v4, v12, v13
	v_cvt_pk_bf16_f32 v5, v14, v15
	v_cvt_pk_bf16_f32 v6, v16, v17
	v_cvt_pk_bf16_f32 v7, v10, v7
	flat_store_dwordx4 v[8:9], v[4:7] sc1 nt
	s_cbranch_vccnz .LBB0_149
	s_andn2_b64 vcc, exec, s[6:7]
	s_cbranch_vccnz .LBB0_148
	s_barrier
	s_branch .LBB0_148
